# MLA: side-job tick behind the stage barrier with the even tile's first K fragment reads issued in front of it (tick covers the LDS latency after the barrier)
# baseline (speedup 1.0000x reference)
; #define LAS __attribute__((address_space(3)))
; DEV float ex2(float x) { return __builtin_amdgcn_exp2f(x); }
; #define MLA_SB() __builtin_amdgcn_sched_barrier(0)
; #define MLA_PIN(x) asm volatile("" : "+v"(x))
; #define MFMA8(a, b, c) __builtin_amdgcn_mfma_scale_f32_32x32x64_f8f6f4((a), (b), (c), 0, 0, 0, 0x7f7f7f7f, 0, 0x7c7c7c7c)
; template <int VAR> DEV void mla_step(f32x16& C0, f32x16& C1, f32x16& P0, f32x16& P1, f32x16& o0, f32x16& o1, f32x16& lacc,
;                   const v8i (&qf)[2], const f32x16& cini, LAS char* kp, LAS char* vp, v8i& pw) {
;     v8i kf[2], vf[2];
;     const v8i ones8 = {0x38383838, 0x38383838, 0x38383838, 0x38383838, 0x38383838, 0x38383838, 0x38383838, 0x38383838};
;     kf[0] = mla_kf8(kp, 0, 0); kf[1] = mla_kf8(kp, 1, 0);
;     MLA_SB();
; #pragma unroll
;     for (int g = 0; g < 4; ++g) {
;         const int kb = g & 1, sx = g >> 1;
;         if (kb) C1 = MFMA8(kf[1], qf[sx], sx == 0 ? cini : C1); else C0 = MFMA8(kf[0], qf[sx], sx == 0 ? cini : C0);
;         if (g < 2) kf[kb] = mla_kf8(kp, kb, 1);
;         if (g >= 2) vf[g - 2] = mla_vf8(vp, g - 2);
; #pragma unroll
;         for (int j = 0; j < 2; ++j) { const int w = 2 * g + j, e = 4 * w;
;             if (VAR == 3) pw[w] = __builtin_bit_cast(int, (e < 16) ? P0[e] : P1[e - 16]);
;             else pw[w] = (int)((e < 16) ? pk_bf8x4(P0[e], P0[e + 1], P0[e + 2], P0[e + 3], pw[w]) : pk_bf8x4(P1[e - 16], P1[e - 15], P1[e - 14], P1[e - 13], pw[w])); }
;         if (g == 3) MLA_PIN(pw);
;         MLA_SB();
;     }
; #pragma unroll
;     for (int g = 0; g < 3; ++g) {
;         if (g == 0) o0 = MFMA8PV(vf[0], pw, o0); else if (g == 1) o1 = MFMA8PV(vf[1], pw, o1); else lacc = MFMA8PV(ones8, pw, lacc);
;         const int e0 = (g * 32) / 3, e1 = ((g + 1) * 32) / 3;
; #pragma unroll
;         for (int e = e0; e < e1; ++e) { if (VAR == 2 || VAR == 3) continue; if (e < 16) C0[e] = ex2(C0[e]); else C1[e - 16] = ex2(C1[e - 16]); }
;         if (g < 2) MLA_PIN(C0);
;         if (g > 0) MLA_PIN(C1);
;         MLA_SB();
;     }
; }
; template <int VAR> DEV void mla_unit(const Params& p, int layer, int b, int hd, int tokbase, int t0, int t1, LAS char* lds, SideJob& sj) {
;     ...
;             { LAS char* nb = lds + nslot * STG; LAS char* ob = lds + slot * STG; mla_step<VAR>(sA0, sA1, sB0, sB1, o0, o1, lacc, qf, cini, nb + koffl, ob + MLA_VSUB + voffl, pw); }
.LBB0_812:
	s_mul_i32 s64, s62, 0x6000
	s_add_i32 s2, s64, 0x6000
	s_cmp_eq_u32 s62, 2
	s_cselect_b32 s2, 0, s2
	s_add_i32 s2, s2, s60
	s_mov_b32 s3, m0
	s_mov_b32 m0, s2
	v_cvt_pk_bf8_f32 v146, v114, v115
	v_cvt_pk_bf8_f32 v147, v118, v119
	v_exp_f32_e32 v101, v101
	v_exp_f32_e32 v102, v102
	v_exp_f32_e32 v103, v103
	s_waitcnt lgkmcnt(1)
	v_mfma_scale_f32_32x32x64_f8f6f4 v[82:97], v[66:73], v[138:145], v[2:17], v209, v208 op_sel_hi:[0,0,0]
	global_load_lds_dwordx4 v[162:163], off
	ds_read_b128 v[164:167], v173 offset:4096
	ds_read_b128 v[168:171], v173 offset:5120
	v_cvt_pk_bf8_f32 v146, v116, v117 op_sel:[0,0,1]
	v_cvt_pk_bf8_f32 v147, v120, v121 op_sel:[0,0,1]
	v_cvt_pk_bf8_f32 v148, v122, v123
	v_cvt_pk_bf8_f32 v149, v126, v127
	ds_read_b128 v[114:117], v173 offset:4608
	ds_read_b128 v[118:121], v173 offset:5632
	v_exp_f32_e32 v104, v104
	v_exp_f32_e32 v105, v105
	s_waitcnt lgkmcnt(4)
	v_mfma_scale_f32_32x32x64_f8f6f4 v[66:81], v[74:81], v[138:145], v[2:17], v209, v208 op_sel_hi:[0,0,0]
	global_load_lds_dwordx4 v[162:163], off offset:1024
	v_cvt_pk_bf8_f32 v148, v124, v125 op_sel:[0,0,1]
	v_cvt_pk_bf8_f32 v149, v128, v129 op_sel:[0,0,1]
	ds_read_b128 v[122:125], v172 offset:20480
	ds_read_b128 v[126:129], v172 offset:21504
	v_exp_f32_e32 v106, v106
	v_exp_f32_e32 v107, v107
	v_exp_f32_e32 v108, v108
	s_waitcnt lgkmcnt(4)
	v_mfma_scale_f32_32x32x64_f8f6f4 v[82:97], v[164:171], v[130:137], v[82:97], v209, v208 op_sel_hi:[0,0,0]
	global_load_lds_dwordx4 v[162:163], off offset:2048
	s_mov_b32 m0, s3
	v_exp_f32_e32 v109, v109
	v_exp_f32_e32 v110, v110
	v_exp_f32_e32 v111, v111
	v_exp_f32_e32 v112, v112
	v_exp_f32_e32 v113, v113
	s_waitcnt lgkmcnt(2)
	v_mfma_scale_f32_32x32x64_f8f6f4 v[66:81], v[114:121], v[130:137], v[66:81], v209, v208 op_sel_hi:[0,0,0]
	v_cvt_pk_bf8_f32 v150, v98, v99
	v_cvt_pk_bf8_f32 v151, v102, v103
	v_cvt_pk_bf8_f32 v150, v100, v101 op_sel:[0,0,1]
	v_cvt_pk_bf8_f32 v151, v104, v105 op_sel:[0,0,1]
	v_cvt_pk_bf8_f32 v152, v106, v107
	v_cvt_pk_bf8_f32 v153, v110, v111
	v_cvt_pk_bf8_f32 v152, v108, v109 op_sel:[0,0,1]
	v_cvt_pk_bf8_f32 v153, v112, v113 op_sel:[0,0,1]
	ds_read_b128 v[98:101], v172 offset:20992
	ds_read_b128 v[102:105], v172 offset:22016
	s_waitcnt lgkmcnt(2)
	v_mfma_scale_f32_32x32x64_f8f6f4 v[50:65], v[122:129], v[146:153], v[50:65], v209, v209 op_sel_hi:[0,0,0] blgp:1
	s_nop 0
	v_exp_f32_e32 v82, v82
	v_exp_f32_e32 v83, v83
	v_exp_f32_e32 v84, v84
	v_exp_f32_e32 v85, v85
	v_exp_f32_e32 v86, v86
	v_exp_f32_e32 v87, v87
	s_waitcnt lgkmcnt(0)
	v_mfma_scale_f32_32x32x64_f8f6f4 v[18:33], v[98:105], v[146:153], v[18:33], v209, v209 op_sel_hi:[0,0,0] blgp:1
	v_exp_f32_e32 v88, v88
	v_exp_f32_e32 v89, v89
	v_exp_f32_e32 v90, v90
	v_exp_f32_e32 v91, v91
	v_exp_f32_e32 v92, v92
	v_exp_f32_e32 v93, v93
	v_mfma_scale_f32_32x32x64_f8f6f4 v[34:49], v[210:217], v[146:153], v[34:49], v209, v209 op_sel_hi:[0,0,0] blgp:1
	v_exp_f32_e32 v94, v94
	v_exp_f32_e32 v95, v95
	v_exp_f32_e32 v96, v96
	v_exp_f32_e32 v97, v97
	v_exp_f32_e32 v66, v66
	v_exp_f32_e32 v67, v67
	v_exp_f32_e32 v68, v68
	s_mov_b64 s[20:21], 0x6000
	s_cmpk_lg_i32 s61, 0x80
	v_lshl_add_u64 v[162:163], v[162:163], 0, s[20:21]
	s_cbranch_scc0 .LBB0_835
; #define LAS __attribute__((address_space(3)))
; #define WAITV(n) asm volatile("s_waitcnt vmcnt(%0)" ::"n"(n) : "memory")
; template <int VAR> DEV void mla_step(f32x16& C0, f32x16& C1, f32x16& P0, f32x16& P1, f32x16& o0, f32x16& o1, f32x16& lacc,
;                   const v8i (&qf)[2], const f32x16& cini, LAS char* kp, LAS char* vp, v8i& pw) {
;     v8i kf[2], vf[2];
;     const v8i ones8 = {0x38383838, 0x38383838, 0x38383838, 0x38383838, 0x38383838, 0x38383838, 0x38383838, 0x38383838};
;     kf[0] = mla_kf8(kp, 0, 0); kf[1] = mla_kf8(kp, 1, 0);
;     MLA_SB();
; #pragma unroll
;     for (int g = 0; g < 4; ++g) {
;         const int kb = g & 1, sx = g >> 1;
;         if (kb) C1 = MFMA8(kf[1], qf[sx], sx == 0 ? cini : C1); else C0 = MFMA8(kf[0], qf[sx], sx == 0 ? cini : C0);
;         if (g < 2) kf[kb] = mla_kf8(kp, kb, 1);
;         if (g >= 2) vf[g - 2] = mla_vf8(vp, g - 2);
; #pragma unroll
;         for (int j = 0; j < 2; ++j) { const int w = 2 * g + j, e = 4 * w;
;             if (VAR == 3) pw[w] = __builtin_bit_cast(int, (e < 16) ? P0[e] : P1[e - 16]);
;             else pw[w] = (int)((e < 16) ? pk_bf8x4(P0[e], P0[e + 1], P0[e + 2], P0[e + 3], pw[w]) : pk_bf8x4(P1[e - 16], P1[e - 15], P1[e - 14], P1[e - 13], pw[w])); }
;         if (g == 3) MLA_PIN(pw);
;         MLA_SB();
;     }
; #pragma unroll
;     for (int g = 0; g < 3; ++g) {
;         if (g == 0) o0 = MFMA8PV(vf[0], pw, o0); else if (g == 1) o1 = MFMA8PV(vf[1], pw, o1); else lacc = MFMA8PV(ones8, pw, lacc);
;         const int e0 = (g * 32) / 3, e1 = ((g + 1) * 32) / 3;
; #pragma unroll
;         for (int e = e0; e < e1; ++e) { if (VAR == 2 || VAR == 3) continue; if (e < 16) C0[e] = ex2(C0[e]); else C1[e - 16] = ex2(C1[e - 16]); }
;         if (g < 2) MLA_PIN(C0);
;         if (g > 0) MLA_PIN(C1);
;         MLA_SB();
;     }
; }
; template <int VAR> DEV void mla_unit(const Params& p, int layer, int b, int hd, int tokbase, int t0, int t1, LAS char* lds, SideJob& sj) {
;     ...
;     for (int s = 0; s < ns; ++s) {
;         sj_tick(p, layer, sj, lds, tid);
;         { LAS char* base = lds + slot * STG; mla_step<VAR>(sB0, sB1, sA0, sA1, o0, o1, lacc, qf, cini, base + MLA_KSUB + koffl, base + voffl, pw); }
;         if (s + 1 < ns) {
;             const int nslot = (slot == 2) ? 0 : slot + 1;
;             WAITV(0); SBAR();
;             if (s + 2 < ns) MLA_ISSUE(t0 + s + 2, (nslot == 2) ? 0 : nslot + 1);
.LBB0_813:
	s_mul_i32 s2, s62, 0x6000
	v_add_u32_e32 v172, s2, v200
	ds_read_b128 v[98:101], v172 offset:8192
	ds_read_b128 v[106:109], v172 offset:8704
	ds_read_b128 v[102:105], v172 offset:9216
	ds_read_b128 v[110:113], v172 offset:9728
	v_cvt_pk_bf8_f32 v146, v82, v83
	v_cvt_pk_bf8_f32 v147, v86, v87
	v_exp_f32_e32 v69, v69
	v_exp_f32_e32 v70, v70
	v_exp_f32_e32 v71, v71
	s_waitcnt lgkmcnt(1)
	v_mfma_scale_f32_32x32x64_f8f6f4 v[114:129], v[98:105], v[138:145], v[2:17], v209, v208 op_sel_hi:[0,0,0]
	ds_read_b128 v[154:157], v172 offset:12288
	ds_read_b128 v[158:161], v172 offset:13312
	v_cvt_pk_bf8_f32 v146, v84, v85 op_sel:[0,0,1]
	v_cvt_pk_bf8_f32 v147, v88, v89 op_sel:[0,0,1]
	v_cvt_pk_bf8_f32 v148, v90, v91
	v_cvt_pk_bf8_f32 v149, v94, v95
	ds_read_b128 v[82:85], v172 offset:12800
	ds_read_b128 v[86:89], v172 offset:13824
	v_exp_f32_e32 v72, v72
	v_exp_f32_e32 v73, v73
	s_waitcnt lgkmcnt(4)
	v_mfma_scale_f32_32x32x64_f8f6f4 v[98:113], v[106:113], v[138:145], v[2:17], v209, v208 op_sel_hi:[0,0,0]
	v_cvt_pk_bf8_f32 v148, v92, v93 op_sel:[0,0,1]
	v_cvt_pk_bf8_f32 v149, v96, v97 op_sel:[0,0,1]
	ds_read_b128 v[90:93], v172 offset:16384
	ds_read_b128 v[94:97], v172 offset:17408
	v_exp_f32_e32 v74, v74
	v_exp_f32_e32 v75, v75
	v_exp_f32_e32 v76, v76
	s_waitcnt lgkmcnt(4)
	v_mfma_scale_f32_32x32x64_f8f6f4 v[114:129], v[154:161], v[130:137], v[114:129], v209, v208 op_sel_hi:[0,0,0]
	v_exp_f32_e32 v77, v77
	v_exp_f32_e32 v78, v78
	v_exp_f32_e32 v79, v79
	v_exp_f32_e32 v80, v80
	v_exp_f32_e32 v81, v81
	s_waitcnt lgkmcnt(2)
	v_mfma_scale_f32_32x32x64_f8f6f4 v[98:113], v[82:89], v[130:137], v[98:113], v209, v208 op_sel_hi:[0,0,0]
	v_cvt_pk_bf8_f32 v150, v66, v67
	v_cvt_pk_bf8_f32 v151, v70, v71
	v_cvt_pk_bf8_f32 v150, v68, v69 op_sel:[0,0,1]
	v_cvt_pk_bf8_f32 v151, v72, v73 op_sel:[0,0,1]
	v_cvt_pk_bf8_f32 v152, v74, v75
	v_cvt_pk_bf8_f32 v153, v78, v79
	v_cvt_pk_bf8_f32 v152, v76, v77 op_sel:[0,0,1]
	v_cvt_pk_bf8_f32 v153, v80, v81 op_sel:[0,0,1]
	ds_read_b128 v[66:69], v172 offset:16896
	ds_read_b128 v[70:73], v172 offset:17920
	s_waitcnt lgkmcnt(2)
	v_mfma_scale_f32_32x32x64_f8f6f4 v[50:65], v[90:97], v[146:153], v[50:65], v209, v209 op_sel_hi:[0,0,0] blgp:1
	s_nop 0
	v_exp_f32_e32 v114, v114
	v_exp_f32_e32 v115, v115
	v_exp_f32_e32 v116, v116
	v_exp_f32_e32 v117, v117
	v_exp_f32_e32 v118, v118
	v_exp_f32_e32 v119, v119
	s_waitcnt lgkmcnt(0)
	v_mfma_scale_f32_32x32x64_f8f6f4 v[18:33], v[66:73], v[146:153], v[18:33], v209, v209 op_sel_hi:[0,0,0] blgp:1
	v_exp_f32_e32 v120, v120
	v_exp_f32_e32 v121, v121
	v_exp_f32_e32 v122, v122
	v_exp_f32_e32 v123, v123
	v_exp_f32_e32 v124, v124
	v_exp_f32_e32 v125, v125
	v_mfma_scale_f32_32x32x64_f8f6f4 v[34:49], v[210:217], v[146:153], v[34:49], v209, v209 op_sel_hi:[0,0,0] blgp:1
	v_exp_f32_e32 v126, v126
	v_exp_f32_e32 v127, v127
	v_exp_f32_e32 v128, v128
	v_exp_f32_e32 v129, v129
	v_exp_f32_e32 v98, v98
	v_exp_f32_e32 v99, v99
	v_exp_f32_e32 v100, v100
	s_add_i32 s61, s61, 1
	s_add_i32 s2, s62, 1
	s_cmp_lg_u32 s62, 2
	s_cselect_b32 s62, s2, 0
	s_mul_i32 s64, s62, 0x6000
	s_add_i32 s2, s64, 0x6000
	s_cmp_eq_u32 s62, 2
	s_cselect_b64 s[8:9], -1, 0
	s_waitcnt vmcnt(0)
	s_and_b64 s[20:21], s[8:9], exec
	s_waitcnt lgkmcnt(0)
	s_barrier
	v_add_u32_e32 v173, s64, v200
	ds_read_b128 v[66:69], v173
	ds_read_b128 v[74:77], v173 offset:512
	ds_read_b128 v[70:73], v173 offset:1024
	ds_read_b128 v[78:81], v173 offset:1536
	s_add_i32 s2, s29, s61
	s_add_i32 s2, s2, -1
	s_and_b32 s63, s2, 3
	s_cmp_gt_i32 s33, 63
	s_cselect_b64 s[8:9], -1, 0
	s_cmp_eq_u32 s63, 3
	s_cselect_b64 s[20:21], -1, 0
	s_or_b64 s[8:9], s[8:9], s[20:21]
	s_and_b64 vcc, exec, s[8:9]
	s_cbranch_vccnz .LBB0_812
	s_add_i32 s20, s33, s12
	s_cmpk_lt_i32 s36, 0x100
	s_cselect_b64 s[50:51], -1, 0
	s_lshl_b32 s58, s36, 6
	s_cmpk_gt_i32 s36, 0xff
	s_mov_b64 s[56:57], -1
	s_cbranch_scc1 .LBB0_816
	s_ashr_i32 s21, s20, 31
	s_lshl_b64 s[52:53], s[20:21], 21
	s_add_u32 s8, s44, s52
	s_addc_u32 s9, s45, s53
	s_add_u32 s52, s46, s52
	s_addc_u32 s53, s47, s53
	s_lshl_b64 s[54:55], s[20:21], 20
	s_add_u32 s54, s13, s54
	s_addc_u32 s55, s16, s55
	s_and_b32 s30, s58, 0x3c0
	s_ashr_i32 s64, s36, 4
	s_mov_b64 s[56:57], 0
